# v13 + loop-edge edit: K-loop counter and pointer updates moved ahead of the closing barrier in five GEMM loops
# baseline (speedup 1.0000x reference)
.LBB0_287:
	ds_read_b128 v[134:137], v198
	ds_read_b128 v[138:141], v198 offset:1024
	ds_read_b128 v[142:145], v198 offset:2048
	ds_read_b128 v[146:149], v198 offset:3072
	ds_read_b128 v[150:153], v199
	ds_read_b128 v[154:157], v199 offset:1024
	ds_read_b128 v[158:161], v199 offset:2048
	ds_read_b128 v[178:181], v199 offset:3072
	s_add_u32 s14, s30, 0xfffc0080
	s_addc_u32 s22, s31, -1
	s_cmp_eq_u32 s70, 12
	s_cselect_b32 s37, s54, s22
	s_cselect_b32 s36, s55, s14
	s_cselect_b32 s23, s56, s69
	s_cselect_b32 s22, s57, s68
	s_mov_b32 m0, s58
	v_lshl_add_u64 v[162:163], s[30:31], 0, v[170:171]
	ds_read_b128 v[182:185], v197
	ds_read_b128 v[190:193], v197 offset:1024
	ds_read_b128 v[200:203], v197 offset:2048
	ds_read_b128 v[204:207], v197 offset:3072
	ds_read_b128 v[208:211], v197 offset:4096
	ds_read_b128 v[212:215], v197 offset:5120
	ds_read_b128 v[216:219], v197 offset:6144
	ds_read_b128 v[222:225], v197 offset:7168
	global_load_lds_dwordx4 v[162:163], off
	v_lshl_add_u64 v[162:163], s[30:31], 0, v[172:173]
	s_mov_b32 m0, s59
	s_nop 0
	global_load_lds_dwordx4 v[162:163], off
	s_waitcnt vmcnt(8)
	s_waitcnt lgkmcnt(0)
	s_barrier
	s_setprio 1
	s_waitcnt lgkmcnt(0)
	v_mfma_f32_16x16x32_bf16 v[128:131], v[134:137], v[182:185], v[128:131]
	v_mfma_f32_16x16x32_bf16 v[124:127], v[142:145], v[182:185], v[124:127]
	v_mfma_f32_16x16x32_bf16 v[116:119], v[142:145], v[200:203], v[116:119]
	v_mfma_f32_16x16x32_bf16 v[120:123], v[134:137], v[200:203], v[120:123]
	v_mfma_f32_16x16x32_bf16 v[112:115], v[134:137], v[208:211], v[112:115]
	v_mfma_f32_16x16x32_bf16 v[108:111], v[142:145], v[208:211], v[108:111]
	v_mfma_f32_16x16x32_bf16 v[100:103], v[142:145], v[216:219], v[100:103]
	v_mfma_f32_16x16x32_bf16 v[104:107], v[134:137], v[216:219], v[104:107]
	v_mfma_f32_16x16x32_bf16 v[128:131], v[138:141], v[190:193], v[128:131]
	v_mfma_f32_16x16x32_bf16 v[124:127], v[146:149], v[190:193], v[124:127]
	v_mfma_f32_16x16x32_bf16 v[116:119], v[146:149], v[204:207], v[116:119]
	v_mfma_f32_16x16x32_bf16 v[120:123], v[138:141], v[204:207], v[120:123]
	v_mfma_f32_16x16x32_bf16 v[112:115], v[138:141], v[212:215], v[112:115]
	v_mfma_f32_16x16x32_bf16 v[108:111], v[146:149], v[212:215], v[108:111]
	v_mfma_f32_16x16x32_bf16 v[100:103], v[146:149], v[222:225], v[100:103]
	v_mfma_f32_16x16x32_bf16 v[104:107], v[138:141], v[222:225], v[104:107]
	s_setprio 0
	s_setprio 1
	v_mfma_f32_16x16x32_bf16 v[96:99], v[150:153], v[182:185], v[96:99]
	v_mfma_f32_16x16x32_bf16 v[92:95], v[158:161], v[182:185], v[92:95]
	v_mfma_f32_16x16x32_bf16 v[84:87], v[158:161], v[200:203], v[84:87]
	v_mfma_f32_16x16x32_bf16 v[88:91], v[150:153], v[200:203], v[88:91]
	v_mfma_f32_16x16x32_bf16 v[80:83], v[150:153], v[208:211], v[80:83]
	v_mfma_f32_16x16x32_bf16 v[76:79], v[158:161], v[208:211], v[76:79]
	v_mfma_f32_16x16x32_bf16 v[68:71], v[158:161], v[216:219], v[68:71]
	v_mfma_f32_16x16x32_bf16 v[72:75], v[150:153], v[216:219], v[72:75]
	v_mfma_f32_16x16x32_bf16 v[96:99], v[154:157], v[190:193], v[96:99]
	v_mfma_f32_16x16x32_bf16 v[92:95], v[178:181], v[190:193], v[92:95]
	v_mfma_f32_16x16x32_bf16 v[84:87], v[178:181], v[204:207], v[84:87]
	v_mfma_f32_16x16x32_bf16 v[88:91], v[154:157], v[204:207], v[88:91]
	v_mfma_f32_16x16x32_bf16 v[80:83], v[154:157], v[212:215], v[80:83]
	v_mfma_f32_16x16x32_bf16 v[76:79], v[178:181], v[212:215], v[76:79]
	v_mfma_f32_16x16x32_bf16 v[68:71], v[178:181], v[222:225], v[68:71]
	v_mfma_f32_16x16x32_bf16 v[72:75], v[154:157], v[222:225], v[72:75]
	s_setprio 0
	s_barrier
	s_mov_b32 m0, s60
	v_lshl_add_u64 v[162:163], s[22:23], 0, v[34:35]
	s_add_u32 s72, s22, 0x40000
	ds_read_b128 v[182:185], v197 offset:16384
	ds_read_b128 v[190:193], v197 offset:17408
	ds_read_b128 v[200:203], v197 offset:18432
	ds_read_b128 v[204:207], v197 offset:19456
	ds_read_b128 v[208:211], v197 offset:20480
	ds_read_b128 v[212:215], v197 offset:21504
	ds_read_b128 v[216:219], v197 offset:22528
	ds_read_b128 v[222:225], v197 offset:23552
	global_load_lds_dwordx4 v[162:163], off
	v_lshl_add_u64 v[174:175], s[22:23], 0, v[164:165]
	s_mov_b32 m0, s61
	s_addc_u32 s73, s23, 0
	global_load_lds_dwordx4 v[174:175], off
	v_lshl_add_u64 v[194:195], s[72:73], 0, v[34:35]
	s_mov_b32 m0, s62
	v_lshl_add_u64 v[226:227], s[36:37], 0, v[166:167]
	global_load_lds_dwordx4 v[194:195], off
	v_lshl_add_u64 v[194:195], s[72:73], 0, v[164:165]
	s_mov_b32 m0, s63
	s_nop 0
	global_load_lds_dwordx4 v[194:195], off
	v_lshl_add_u64 v[194:195], s[36:37], 0, v[168:169]
	s_mov_b32 m0, s41
	s_nop 0
	global_load_lds_dwordx4 v[194:195], off
	s_mov_b32 m0, s42
	s_nop 0
	global_load_lds_dwordx4 v[226:227], off
	s_waitcnt vmcnt(8)
	s_waitcnt lgkmcnt(0)
	s_barrier
	s_setprio 1
	s_waitcnt lgkmcnt(0)
	v_mfma_f32_16x16x32_bf16 v[64:67], v[134:137], v[182:185], v[64:67]
	v_mfma_f32_16x16x32_bf16 v[60:63], v[142:145], v[182:185], v[60:63]
	v_mfma_f32_16x16x32_bf16 v[52:55], v[142:145], v[200:203], v[52:55]
	v_mfma_f32_16x16x32_bf16 v[56:59], v[134:137], v[200:203], v[56:59]
	v_mfma_f32_16x16x32_bf16 v[48:51], v[134:137], v[208:211], v[48:51]
	v_mfma_f32_16x16x32_bf16 v[44:47], v[142:145], v[208:211], v[44:47]
	v_mfma_f32_16x16x32_bf16 v[36:39], v[142:145], v[216:219], v[36:39]
	v_mfma_f32_16x16x32_bf16 v[40:43], v[134:137], v[216:219], v[40:43]
	v_mfma_f32_16x16x32_bf16 v[64:67], v[138:141], v[190:193], v[64:67]
	v_mfma_f32_16x16x32_bf16 v[60:63], v[146:149], v[190:193], v[60:63]
	v_mfma_f32_16x16x32_bf16 v[52:55], v[146:149], v[204:207], v[52:55]
	v_mfma_f32_16x16x32_bf16 v[56:59], v[138:141], v[204:207], v[56:59]
	v_mfma_f32_16x16x32_bf16 v[48:51], v[138:141], v[212:215], v[48:51]
	v_mfma_f32_16x16x32_bf16 v[44:47], v[146:149], v[212:215], v[44:47]
	v_mfma_f32_16x16x32_bf16 v[36:39], v[146:149], v[222:225], v[36:39]
	v_mfma_f32_16x16x32_bf16 v[40:43], v[138:141], v[222:225], v[40:43]
	s_setprio 0
	s_setprio 1
	v_mfma_f32_16x16x32_bf16 v[30:33], v[150:153], v[182:185], v[30:33]
	v_mfma_f32_16x16x32_bf16 v[26:29], v[158:161], v[182:185], v[26:29]
	v_mfma_f32_16x16x32_bf16 v[18:21], v[158:161], v[200:203], v[18:21]
	v_mfma_f32_16x16x32_bf16 v[22:25], v[150:153], v[200:203], v[22:25]
	v_mfma_f32_16x16x32_bf16 v[14:17], v[150:153], v[208:211], v[14:17]
	v_mfma_f32_16x16x32_bf16 v[10:13], v[158:161], v[208:211], v[10:13]
	v_mfma_f32_16x16x32_bf16 v[2:5], v[158:161], v[216:219], v[2:5]
	v_mfma_f32_16x16x32_bf16 v[6:9], v[150:153], v[216:219], v[6:9]
	v_mfma_f32_16x16x32_bf16 v[30:33], v[154:157], v[190:193], v[30:33]
	v_mfma_f32_16x16x32_bf16 v[26:29], v[178:181], v[190:193], v[26:29]
	v_mfma_f32_16x16x32_bf16 v[18:21], v[178:181], v[204:207], v[18:21]
	v_mfma_f32_16x16x32_bf16 v[22:25], v[154:157], v[204:207], v[22:25]
	v_mfma_f32_16x16x32_bf16 v[14:17], v[154:157], v[212:215], v[14:17]
	v_mfma_f32_16x16x32_bf16 v[10:13], v[178:181], v[212:215], v[10:13]
	v_mfma_f32_16x16x32_bf16 v[2:5], v[178:181], v[222:225], v[2:5]
	v_mfma_f32_16x16x32_bf16 v[6:9], v[154:157], v[222:225], v[6:9]
	s_setprio 0
	s_barrier
	ds_read_b128 v[134:137], v132
	ds_read_b128 v[138:141], v132 offset:1024
	ds_read_b128 v[142:145], v132 offset:2048
	ds_read_b128 v[146:149], v132 offset:3072
	ds_read_b128 v[150:153], v133
	ds_read_b128 v[154:157], v133 offset:1024
	ds_read_b128 v[158:161], v133 offset:2048
	ds_read_b128 v[178:181], v133 offset:3072
	s_add_u32 s36, s36, 0x40000
	s_addc_u32 s37, s37, 0
	s_mov_b32 m0, s43
	v_lshl_add_u64 v[228:229], s[36:37], 0, v[168:169]
	ds_read_b128 v[182:185], v197 offset:32768
	ds_read_b128 v[190:193], v197 offset:33792
	ds_read_b128 v[200:203], v197 offset:34816
	ds_read_b128 v[204:207], v197 offset:35840
	ds_read_b128 v[208:211], v197 offset:36864
	ds_read_b128 v[212:215], v197 offset:37888
	ds_read_b128 v[216:219], v197 offset:38912
	ds_read_b128 v[222:225], v197 offset:39936
	global_load_lds_dwordx4 v[228:229], off
	v_lshl_add_u64 v[228:229], s[36:37], 0, v[166:167]
	s_mov_b32 m0, s44
	s_nop 0
	global_load_lds_dwordx4 v[228:229], off
	s_waitcnt vmcnt(8)
	s_waitcnt lgkmcnt(0)
	s_barrier
	s_setprio 1
	s_waitcnt lgkmcnt(0)
	v_mfma_f32_16x16x32_bf16 v[128:131], v[134:137], v[182:185], v[128:131]
	v_mfma_f32_16x16x32_bf16 v[124:127], v[142:145], v[182:185], v[124:127]
	v_mfma_f32_16x16x32_bf16 v[116:119], v[142:145], v[200:203], v[116:119]
	v_mfma_f32_16x16x32_bf16 v[120:123], v[134:137], v[200:203], v[120:123]
	v_mfma_f32_16x16x32_bf16 v[112:115], v[134:137], v[208:211], v[112:115]
	v_mfma_f32_16x16x32_bf16 v[108:111], v[142:145], v[208:211], v[108:111]
	v_mfma_f32_16x16x32_bf16 v[100:103], v[142:145], v[216:219], v[100:103]
	v_mfma_f32_16x16x32_bf16 v[104:107], v[134:137], v[216:219], v[104:107]
	v_mfma_f32_16x16x32_bf16 v[128:131], v[138:141], v[190:193], v[128:131]
	v_mfma_f32_16x16x32_bf16 v[124:127], v[146:149], v[190:193], v[124:127]
	v_mfma_f32_16x16x32_bf16 v[116:119], v[146:149], v[204:207], v[116:119]
	v_mfma_f32_16x16x32_bf16 v[120:123], v[138:141], v[204:207], v[120:123]
	v_mfma_f32_16x16x32_bf16 v[112:115], v[138:141], v[212:215], v[112:115]
	v_mfma_f32_16x16x32_bf16 v[108:111], v[146:149], v[212:215], v[108:111]
	v_mfma_f32_16x16x32_bf16 v[100:103], v[146:149], v[222:225], v[100:103]
	v_mfma_f32_16x16x32_bf16 v[104:107], v[138:141], v[222:225], v[104:107]
	s_setprio 0
	s_setprio 1
	v_mfma_f32_16x16x32_bf16 v[96:99], v[150:153], v[182:185], v[96:99]
	v_mfma_f32_16x16x32_bf16 v[92:95], v[158:161], v[182:185], v[92:95]
	v_mfma_f32_16x16x32_bf16 v[84:87], v[158:161], v[200:203], v[84:87]
	v_mfma_f32_16x16x32_bf16 v[88:91], v[150:153], v[200:203], v[88:91]
	v_mfma_f32_16x16x32_bf16 v[80:83], v[150:153], v[208:211], v[80:83]
	v_mfma_f32_16x16x32_bf16 v[76:79], v[158:161], v[208:211], v[76:79]
	v_mfma_f32_16x16x32_bf16 v[68:71], v[158:161], v[216:219], v[68:71]
	v_mfma_f32_16x16x32_bf16 v[72:75], v[150:153], v[216:219], v[72:75]
	v_mfma_f32_16x16x32_bf16 v[96:99], v[154:157], v[190:193], v[96:99]
	v_mfma_f32_16x16x32_bf16 v[92:95], v[178:181], v[190:193], v[92:95]
	v_mfma_f32_16x16x32_bf16 v[84:87], v[178:181], v[204:207], v[84:87]
	v_mfma_f32_16x16x32_bf16 v[88:91], v[154:157], v[204:207], v[88:91]
	v_mfma_f32_16x16x32_bf16 v[80:83], v[154:157], v[212:215], v[80:83]
	v_mfma_f32_16x16x32_bf16 v[76:79], v[178:181], v[212:215], v[76:79]
	v_mfma_f32_16x16x32_bf16 v[68:71], v[178:181], v[222:225], v[68:71]
	v_mfma_f32_16x16x32_bf16 v[72:75], v[154:157], v[222:225], v[72:75]
	s_setprio 0
	s_barrier
	s_mov_b32 m0, s64
	v_lshl_add_u64 v[162:163], v[162:163], 0, s[18:19]
	s_add_u32 s22, s22, 0x40080
	ds_read_b128 v[182:185], v197 offset:49152
	ds_read_b128 v[190:193], v197 offset:50176
	ds_read_b128 v[200:203], v197 offset:51200
	ds_read_b128 v[204:207], v197 offset:52224
	ds_read_b128 v[208:211], v197 offset:53248
	ds_read_b128 v[212:215], v197 offset:54272
	ds_read_b128 v[216:219], v197 offset:55296
	ds_read_b128 v[222:225], v197 offset:56320
	global_load_lds_dwordx4 v[162:163], off
	v_lshl_add_u64 v[162:163], v[174:175], 0, s[18:19]
	s_mov_b32 m0, s65
	s_addc_u32 s23, s23, 0
	global_load_lds_dwordx4 v[162:163], off
	v_lshl_add_u64 v[162:163], s[22:23], 0, v[34:35]
	s_mov_b32 m0, s66
	s_nop 0
	global_load_lds_dwordx4 v[162:163], off
	v_lshl_add_u64 v[162:163], s[22:23], 0, v[164:165]
	s_mov_b32 m0, s67
	s_nop 0
	global_load_lds_dwordx4 v[162:163], off
	v_lshl_add_u64 v[162:163], v[194:195], 0, s[18:19]
	s_mov_b32 m0, s47
	s_nop 0
	global_load_lds_dwordx4 v[162:163], off
	v_lshl_add_u64 v[162:163], v[226:227], 0, s[18:19]
	s_mov_b32 m0, s48
	s_nop 0
	global_load_lds_dwordx4 v[162:163], off
	s_waitcnt vmcnt(8)
	s_waitcnt lgkmcnt(0)
	s_barrier
	s_setprio 1
	s_waitcnt lgkmcnt(0)
	v_mfma_f32_16x16x32_bf16 v[64:67], v[134:137], v[182:185], v[64:67]
	v_mfma_f32_16x16x32_bf16 v[60:63], v[142:145], v[182:185], v[60:63]
	v_mfma_f32_16x16x32_bf16 v[52:55], v[142:145], v[200:203], v[52:55]
	v_mfma_f32_16x16x32_bf16 v[56:59], v[134:137], v[200:203], v[56:59]
	v_mfma_f32_16x16x32_bf16 v[48:51], v[134:137], v[208:211], v[48:51]
	v_mfma_f32_16x16x32_bf16 v[44:47], v[142:145], v[208:211], v[44:47]
	v_mfma_f32_16x16x32_bf16 v[36:39], v[142:145], v[216:219], v[36:39]
	v_mfma_f32_16x16x32_bf16 v[40:43], v[134:137], v[216:219], v[40:43]
	v_mfma_f32_16x16x32_bf16 v[64:67], v[138:141], v[190:193], v[64:67]
	v_mfma_f32_16x16x32_bf16 v[60:63], v[146:149], v[190:193], v[60:63]
	v_mfma_f32_16x16x32_bf16 v[52:55], v[146:149], v[204:207], v[52:55]
	v_mfma_f32_16x16x32_bf16 v[56:59], v[138:141], v[204:207], v[56:59]
	v_mfma_f32_16x16x32_bf16 v[48:51], v[138:141], v[212:215], v[48:51]
	v_mfma_f32_16x16x32_bf16 v[44:47], v[146:149], v[212:215], v[44:47]
	v_mfma_f32_16x16x32_bf16 v[36:39], v[146:149], v[222:225], v[36:39]
	v_mfma_f32_16x16x32_bf16 v[40:43], v[138:141], v[222:225], v[40:43]
	s_setprio 0
	s_setprio 1
	v_mfma_f32_16x16x32_bf16 v[30:33], v[150:153], v[182:185], v[30:33]
	v_mfma_f32_16x16x32_bf16 v[26:29], v[158:161], v[182:185], v[26:29]
	v_mfma_f32_16x16x32_bf16 v[18:21], v[158:161], v[200:203], v[18:21]
	v_mfma_f32_16x16x32_bf16 v[22:25], v[150:153], v[200:203], v[22:25]
	v_mfma_f32_16x16x32_bf16 v[14:17], v[150:153], v[208:211], v[14:17]
	v_mfma_f32_16x16x32_bf16 v[10:13], v[158:161], v[208:211], v[10:13]
	v_mfma_f32_16x16x32_bf16 v[2:5], v[158:161], v[216:219], v[2:5]
	v_mfma_f32_16x16x32_bf16 v[6:9], v[150:153], v[216:219], v[6:9]
	v_mfma_f32_16x16x32_bf16 v[30:33], v[154:157], v[190:193], v[30:33]
	v_mfma_f32_16x16x32_bf16 v[26:29], v[178:181], v[190:193], v[26:29]
	v_mfma_f32_16x16x32_bf16 v[18:21], v[178:181], v[204:207], v[18:21]
	v_mfma_f32_16x16x32_bf16 v[22:25], v[154:157], v[204:207], v[22:25]
	v_mfma_f32_16x16x32_bf16 v[14:17], v[154:157], v[212:215], v[14:17]
	v_mfma_f32_16x16x32_bf16 v[10:13], v[178:181], v[212:215], v[10:13]
	v_mfma_f32_16x16x32_bf16 v[2:5], v[178:181], v[222:225], v[2:5]
	v_mfma_f32_16x16x32_bf16 v[6:9], v[154:157], v[222:225], v[6:9]
	s_add_i32 s70, s70, 2
	s_add_u32 s30, s30, 0x100
	s_addc_u32 s31, s31, 0
	s_add_u32 s68, s68, 0x100
	s_addc_u32 s69, s69, 0
	s_cmp_gt_u32 s70, 13
	s_setprio 0
	s_barrier
	s_cbranch_scc0 .LBB0_287
	s_and_b64 vcc, exec, s[8:9]
	s_cbranch_vccz .LBB0_290
	s_barrier

.LBB0_541:
	ds_read_b128 v[134:137], v172
	ds_read_b128 v[138:141], v172 offset:1024
	ds_read_b128 v[142:145], v172 offset:2048
	ds_read_b128 v[146:149], v172 offset:3072
	ds_read_b128 v[150:153], v173
	ds_read_b128 v[154:157], v173 offset:1024
	ds_read_b128 v[158:161], v173 offset:2048
	ds_read_b128 v[162:165], v173 offset:3072
	s_add_u32 s14, s36, 0xfffc0080
	s_addc_u32 s30, s37, -1
	s_cmp_eq_u32 s74, 12
	s_cselect_b32 s41, s58, s30
	s_cselect_b32 s40, s59, s14
	s_cselect_b32 s31, s60, s73
	s_cselect_b32 s30, s61, s72
	s_mov_b32 m0, s62
	v_lshl_add_u64 v[170:171], s[36:37], 0, v[196:197]
	ds_read_b128 v[166:169], v223
	ds_read_b128 v[178:181], v223 offset:1024
	ds_read_b128 v[182:185], v223 offset:2048
	ds_read_b128 v[200:203], v223 offset:3072
	ds_read_b128 v[204:207], v223 offset:4096
	ds_read_b128 v[208:211], v223 offset:5120
	ds_read_b128 v[212:215], v223 offset:6144
	ds_read_b128 v[216:219], v223 offset:7168
	global_load_lds_dwordx4 v[170:171], off
	v_lshl_add_u64 v[170:171], s[36:37], 0, v[198:199]
	s_mov_b32 m0, s63
	s_nop 0
	global_load_lds_dwordx4 v[170:171], off
	s_waitcnt vmcnt(8)
	s_waitcnt lgkmcnt(0)
	s_barrier
	s_setprio 1
	s_waitcnt lgkmcnt(0)
	v_mfma_f32_16x16x32_bf16 v[128:131], v[134:137], v[166:169], v[128:131]
	v_mfma_f32_16x16x32_bf16 v[124:127], v[142:145], v[166:169], v[124:127]
	v_mfma_f32_16x16x32_bf16 v[116:119], v[142:145], v[182:185], v[116:119]
	v_mfma_f32_16x16x32_bf16 v[120:123], v[134:137], v[182:185], v[120:123]
	v_mfma_f32_16x16x32_bf16 v[112:115], v[134:137], v[204:207], v[112:115]
	v_mfma_f32_16x16x32_bf16 v[108:111], v[142:145], v[204:207], v[108:111]
	v_mfma_f32_16x16x32_bf16 v[100:103], v[142:145], v[212:215], v[100:103]
	v_mfma_f32_16x16x32_bf16 v[104:107], v[134:137], v[212:215], v[104:107]
	v_mfma_f32_16x16x32_bf16 v[128:131], v[138:141], v[178:181], v[128:131]
	v_mfma_f32_16x16x32_bf16 v[124:127], v[146:149], v[178:181], v[124:127]
	v_mfma_f32_16x16x32_bf16 v[116:119], v[146:149], v[200:203], v[116:119]
	v_mfma_f32_16x16x32_bf16 v[120:123], v[138:141], v[200:203], v[120:123]
	v_mfma_f32_16x16x32_bf16 v[112:115], v[138:141], v[208:211], v[112:115]
	v_mfma_f32_16x16x32_bf16 v[108:111], v[146:149], v[208:211], v[108:111]
	v_mfma_f32_16x16x32_bf16 v[100:103], v[146:149], v[216:219], v[100:103]
	v_mfma_f32_16x16x32_bf16 v[104:107], v[138:141], v[216:219], v[104:107]
	s_setprio 0
	s_setprio 1
	v_mfma_f32_16x16x32_bf16 v[96:99], v[150:153], v[166:169], v[96:99]
	v_mfma_f32_16x16x32_bf16 v[92:95], v[158:161], v[166:169], v[92:95]
	v_mfma_f32_16x16x32_bf16 v[84:87], v[158:161], v[182:185], v[84:87]
	v_mfma_f32_16x16x32_bf16 v[88:91], v[150:153], v[182:185], v[88:91]
	v_mfma_f32_16x16x32_bf16 v[80:83], v[150:153], v[204:207], v[80:83]
	v_mfma_f32_16x16x32_bf16 v[76:79], v[158:161], v[204:207], v[76:79]
	v_mfma_f32_16x16x32_bf16 v[68:71], v[158:161], v[212:215], v[68:71]
	v_mfma_f32_16x16x32_bf16 v[72:75], v[150:153], v[212:215], v[72:75]
	v_mfma_f32_16x16x32_bf16 v[96:99], v[154:157], v[178:181], v[96:99]
	v_mfma_f32_16x16x32_bf16 v[92:95], v[162:165], v[178:181], v[92:95]
	v_mfma_f32_16x16x32_bf16 v[84:87], v[162:165], v[200:203], v[84:87]
	v_mfma_f32_16x16x32_bf16 v[88:91], v[154:157], v[200:203], v[88:91]
	v_mfma_f32_16x16x32_bf16 v[80:83], v[154:157], v[208:211], v[80:83]
	v_mfma_f32_16x16x32_bf16 v[76:79], v[162:165], v[208:211], v[76:79]
	v_mfma_f32_16x16x32_bf16 v[68:71], v[162:165], v[216:219], v[68:71]
	v_mfma_f32_16x16x32_bf16 v[72:75], v[154:157], v[216:219], v[72:75]
	s_setprio 0
	s_barrier
	s_mov_b32 m0, s64
	v_lshl_add_u64 v[170:171], s[30:31], 0, v[34:35]
	s_add_u32 s76, s30, 0x40000
	ds_read_b128 v[166:169], v223 offset:16384
	ds_read_b128 v[178:181], v223 offset:17408
	ds_read_b128 v[182:185], v223 offset:18432
	ds_read_b128 v[200:203], v223 offset:19456
	ds_read_b128 v[204:207], v223 offset:20480
	ds_read_b128 v[208:211], v223 offset:21504
	ds_read_b128 v[212:215], v223 offset:22528
	ds_read_b128 v[216:219], v223 offset:23552
	global_load_lds_dwordx4 v[170:171], off
	v_lshl_add_u64 v[174:175], s[30:31], 0, v[190:191]
	s_mov_b32 m0, s65
	s_addc_u32 s77, s31, 0
	global_load_lds_dwordx4 v[174:175], off
	v_lshl_add_u64 v[224:225], s[76:77], 0, v[34:35]
	s_mov_b32 m0, s66
	v_lshl_add_u64 v[226:227], s[40:41], 0, v[192:193]
	global_load_lds_dwordx4 v[224:225], off
	v_lshl_add_u64 v[224:225], s[76:77], 0, v[190:191]
	s_mov_b32 m0, s67
	s_nop 0
	global_load_lds_dwordx4 v[224:225], off
	v_lshl_add_u64 v[224:225], s[40:41], 0, v[194:195]
	s_mov_b32 m0, s43
	s_nop 0
	global_load_lds_dwordx4 v[224:225], off
	s_mov_b32 m0, s44
	s_nop 0
	global_load_lds_dwordx4 v[226:227], off
	s_waitcnt vmcnt(8)
	s_waitcnt lgkmcnt(0)
	s_barrier
	s_setprio 1
	s_waitcnt lgkmcnt(0)
	v_mfma_f32_16x16x32_bf16 v[64:67], v[134:137], v[166:169], v[64:67]
	v_mfma_f32_16x16x32_bf16 v[60:63], v[142:145], v[166:169], v[60:63]
	v_mfma_f32_16x16x32_bf16 v[52:55], v[142:145], v[182:185], v[52:55]
	v_mfma_f32_16x16x32_bf16 v[56:59], v[134:137], v[182:185], v[56:59]
	v_mfma_f32_16x16x32_bf16 v[48:51], v[134:137], v[204:207], v[48:51]
	v_mfma_f32_16x16x32_bf16 v[44:47], v[142:145], v[204:207], v[44:47]
	v_mfma_f32_16x16x32_bf16 v[36:39], v[142:145], v[212:215], v[36:39]
	v_mfma_f32_16x16x32_bf16 v[40:43], v[134:137], v[212:215], v[40:43]
	v_mfma_f32_16x16x32_bf16 v[64:67], v[138:141], v[178:181], v[64:67]
	v_mfma_f32_16x16x32_bf16 v[60:63], v[146:149], v[178:181], v[60:63]
	v_mfma_f32_16x16x32_bf16 v[52:55], v[146:149], v[200:203], v[52:55]
	v_mfma_f32_16x16x32_bf16 v[56:59], v[138:141], v[200:203], v[56:59]
	v_mfma_f32_16x16x32_bf16 v[48:51], v[138:141], v[208:211], v[48:51]
	v_mfma_f32_16x16x32_bf16 v[44:47], v[146:149], v[208:211], v[44:47]
	v_mfma_f32_16x16x32_bf16 v[36:39], v[146:149], v[216:219], v[36:39]
	v_mfma_f32_16x16x32_bf16 v[40:43], v[138:141], v[216:219], v[40:43]
	s_setprio 0
	s_setprio 1
	v_mfma_f32_16x16x32_bf16 v[30:33], v[150:153], v[166:169], v[30:33]
	v_mfma_f32_16x16x32_bf16 v[26:29], v[158:161], v[166:169], v[26:29]
	v_mfma_f32_16x16x32_bf16 v[18:21], v[158:161], v[182:185], v[18:21]
	v_mfma_f32_16x16x32_bf16 v[22:25], v[150:153], v[182:185], v[22:25]
	v_mfma_f32_16x16x32_bf16 v[14:17], v[150:153], v[204:207], v[14:17]
	v_mfma_f32_16x16x32_bf16 v[10:13], v[158:161], v[204:207], v[10:13]
	v_mfma_f32_16x16x32_bf16 v[2:5], v[158:161], v[212:215], v[2:5]
	v_mfma_f32_16x16x32_bf16 v[6:9], v[150:153], v[212:215], v[6:9]
	v_mfma_f32_16x16x32_bf16 v[30:33], v[154:157], v[178:181], v[30:33]
	v_mfma_f32_16x16x32_bf16 v[26:29], v[162:165], v[178:181], v[26:29]
	v_mfma_f32_16x16x32_bf16 v[18:21], v[162:165], v[200:203], v[18:21]
	v_mfma_f32_16x16x32_bf16 v[22:25], v[154:157], v[200:203], v[22:25]
	v_mfma_f32_16x16x32_bf16 v[14:17], v[154:157], v[208:211], v[14:17]
	v_mfma_f32_16x16x32_bf16 v[10:13], v[162:165], v[208:211], v[10:13]
	v_mfma_f32_16x16x32_bf16 v[2:5], v[162:165], v[216:219], v[2:5]
	v_mfma_f32_16x16x32_bf16 v[6:9], v[154:157], v[216:219], v[6:9]
	s_setprio 0
	s_barrier
	ds_read_b128 v[134:137], v132
	ds_read_b128 v[138:141], v132 offset:1024
	ds_read_b128 v[142:145], v132 offset:2048
	ds_read_b128 v[146:149], v132 offset:3072
	ds_read_b128 v[150:153], v133
	ds_read_b128 v[154:157], v133 offset:1024
	ds_read_b128 v[158:161], v133 offset:2048
	ds_read_b128 v[162:165], v133 offset:3072
	s_add_u32 s40, s40, 0x40000
	s_addc_u32 s41, s41, 0
	s_mov_b32 m0, s45
	v_lshl_add_u64 v[228:229], s[40:41], 0, v[194:195]
	ds_read_b128 v[166:169], v223 offset:32768
	ds_read_b128 v[178:181], v223 offset:33792
	ds_read_b128 v[182:185], v223 offset:34816
	ds_read_b128 v[200:203], v223 offset:35840
	ds_read_b128 v[204:207], v223 offset:36864
	ds_read_b128 v[208:211], v223 offset:37888
	ds_read_b128 v[212:215], v223 offset:38912
	ds_read_b128 v[216:219], v223 offset:39936
	global_load_lds_dwordx4 v[228:229], off
	v_lshl_add_u64 v[228:229], s[40:41], 0, v[192:193]
	s_mov_b32 m0, s46
	s_nop 0
	global_load_lds_dwordx4 v[228:229], off
	s_waitcnt vmcnt(8)
	s_waitcnt lgkmcnt(0)
	s_barrier
	s_setprio 1
	s_waitcnt lgkmcnt(0)
	v_mfma_f32_16x16x32_bf16 v[128:131], v[134:137], v[166:169], v[128:131]
	v_mfma_f32_16x16x32_bf16 v[124:127], v[142:145], v[166:169], v[124:127]
	v_mfma_f32_16x16x32_bf16 v[116:119], v[142:145], v[182:185], v[116:119]
	v_mfma_f32_16x16x32_bf16 v[120:123], v[134:137], v[182:185], v[120:123]
	v_mfma_f32_16x16x32_bf16 v[112:115], v[134:137], v[204:207], v[112:115]
	v_mfma_f32_16x16x32_bf16 v[108:111], v[142:145], v[204:207], v[108:111]
	v_mfma_f32_16x16x32_bf16 v[100:103], v[142:145], v[212:215], v[100:103]
	v_mfma_f32_16x16x32_bf16 v[104:107], v[134:137], v[212:215], v[104:107]
	v_mfma_f32_16x16x32_bf16 v[128:131], v[138:141], v[178:181], v[128:131]
	v_mfma_f32_16x16x32_bf16 v[124:127], v[146:149], v[178:181], v[124:127]
	v_mfma_f32_16x16x32_bf16 v[116:119], v[146:149], v[200:203], v[116:119]
	v_mfma_f32_16x16x32_bf16 v[120:123], v[138:141], v[200:203], v[120:123]
	v_mfma_f32_16x16x32_bf16 v[112:115], v[138:141], v[208:211], v[112:115]
	v_mfma_f32_16x16x32_bf16 v[108:111], v[146:149], v[208:211], v[108:111]
	v_mfma_f32_16x16x32_bf16 v[100:103], v[146:149], v[216:219], v[100:103]
	v_mfma_f32_16x16x32_bf16 v[104:107], v[138:141], v[216:219], v[104:107]
	s_setprio 0
	s_setprio 1
	v_mfma_f32_16x16x32_bf16 v[96:99], v[150:153], v[166:169], v[96:99]
	v_mfma_f32_16x16x32_bf16 v[92:95], v[158:161], v[166:169], v[92:95]
	v_mfma_f32_16x16x32_bf16 v[84:87], v[158:161], v[182:185], v[84:87]
	v_mfma_f32_16x16x32_bf16 v[88:91], v[150:153], v[182:185], v[88:91]
	v_mfma_f32_16x16x32_bf16 v[80:83], v[150:153], v[204:207], v[80:83]
	v_mfma_f32_16x16x32_bf16 v[76:79], v[158:161], v[204:207], v[76:79]
	v_mfma_f32_16x16x32_bf16 v[68:71], v[158:161], v[212:215], v[68:71]
	v_mfma_f32_16x16x32_bf16 v[72:75], v[150:153], v[212:215], v[72:75]
	v_mfma_f32_16x16x32_bf16 v[96:99], v[154:157], v[178:181], v[96:99]
	v_mfma_f32_16x16x32_bf16 v[92:95], v[162:165], v[178:181], v[92:95]
	v_mfma_f32_16x16x32_bf16 v[84:87], v[162:165], v[200:203], v[84:87]
	v_mfma_f32_16x16x32_bf16 v[88:91], v[154:157], v[200:203], v[88:91]
	v_mfma_f32_16x16x32_bf16 v[80:83], v[154:157], v[208:211], v[80:83]
	v_mfma_f32_16x16x32_bf16 v[76:79], v[162:165], v[208:211], v[76:79]
	v_mfma_f32_16x16x32_bf16 v[68:71], v[162:165], v[216:219], v[68:71]
	v_mfma_f32_16x16x32_bf16 v[72:75], v[154:157], v[216:219], v[72:75]
	s_setprio 0
	s_barrier
	s_mov_b32 m0, s68
	v_lshl_add_u64 v[170:171], v[170:171], 0, s[18:19]
	s_add_u32 s30, s30, 0x40080
	ds_read_b128 v[166:169], v223 offset:49152
	ds_read_b128 v[178:181], v223 offset:50176
	ds_read_b128 v[182:185], v223 offset:51200
	ds_read_b128 v[200:203], v223 offset:52224
	ds_read_b128 v[204:207], v223 offset:53248
	ds_read_b128 v[208:211], v223 offset:54272
	ds_read_b128 v[212:215], v223 offset:55296
	ds_read_b128 v[216:219], v223 offset:56320
	global_load_lds_dwordx4 v[170:171], off
	v_lshl_add_u64 v[170:171], v[174:175], 0, s[18:19]
	s_mov_b32 m0, s69
	s_addc_u32 s31, s31, 0
	global_load_lds_dwordx4 v[170:171], off
	v_lshl_add_u64 v[170:171], s[30:31], 0, v[34:35]
	s_mov_b32 m0, s70
	s_nop 0
	global_load_lds_dwordx4 v[170:171], off
	v_lshl_add_u64 v[170:171], s[30:31], 0, v[190:191]
	s_mov_b32 m0, s71
	s_nop 0
	global_load_lds_dwordx4 v[170:171], off
	v_lshl_add_u64 v[170:171], v[224:225], 0, s[18:19]
	s_mov_b32 m0, s51
	s_nop 0
	global_load_lds_dwordx4 v[170:171], off
	v_lshl_add_u64 v[170:171], v[226:227], 0, s[18:19]
	s_mov_b32 m0, s52
	s_nop 0
	global_load_lds_dwordx4 v[170:171], off
	s_waitcnt vmcnt(8)
	s_waitcnt lgkmcnt(0)
	s_barrier
	s_setprio 1
	s_waitcnt lgkmcnt(0)
	v_mfma_f32_16x16x32_bf16 v[64:67], v[134:137], v[166:169], v[64:67]
	v_mfma_f32_16x16x32_bf16 v[60:63], v[142:145], v[166:169], v[60:63]
	v_mfma_f32_16x16x32_bf16 v[52:55], v[142:145], v[182:185], v[52:55]
	v_mfma_f32_16x16x32_bf16 v[56:59], v[134:137], v[182:185], v[56:59]
	v_mfma_f32_16x16x32_bf16 v[48:51], v[134:137], v[204:207], v[48:51]
	v_mfma_f32_16x16x32_bf16 v[44:47], v[142:145], v[204:207], v[44:47]
	v_mfma_f32_16x16x32_bf16 v[36:39], v[142:145], v[212:215], v[36:39]
	v_mfma_f32_16x16x32_bf16 v[40:43], v[134:137], v[212:215], v[40:43]
	v_mfma_f32_16x16x32_bf16 v[64:67], v[138:141], v[178:181], v[64:67]
	v_mfma_f32_16x16x32_bf16 v[60:63], v[146:149], v[178:181], v[60:63]
	v_mfma_f32_16x16x32_bf16 v[52:55], v[146:149], v[200:203], v[52:55]
	v_mfma_f32_16x16x32_bf16 v[56:59], v[138:141], v[200:203], v[56:59]
	v_mfma_f32_16x16x32_bf16 v[48:51], v[138:141], v[208:211], v[48:51]
	v_mfma_f32_16x16x32_bf16 v[44:47], v[146:149], v[208:211], v[44:47]
	v_mfma_f32_16x16x32_bf16 v[36:39], v[146:149], v[216:219], v[36:39]
	v_mfma_f32_16x16x32_bf16 v[40:43], v[138:141], v[216:219], v[40:43]
	s_setprio 0
	s_setprio 1
	v_mfma_f32_16x16x32_bf16 v[30:33], v[150:153], v[166:169], v[30:33]
	v_mfma_f32_16x16x32_bf16 v[26:29], v[158:161], v[166:169], v[26:29]
	v_mfma_f32_16x16x32_bf16 v[18:21], v[158:161], v[182:185], v[18:21]
	v_mfma_f32_16x16x32_bf16 v[22:25], v[150:153], v[182:185], v[22:25]
	v_mfma_f32_16x16x32_bf16 v[14:17], v[150:153], v[204:207], v[14:17]
	v_mfma_f32_16x16x32_bf16 v[10:13], v[158:161], v[204:207], v[10:13]
	v_mfma_f32_16x16x32_bf16 v[2:5], v[158:161], v[212:215], v[2:5]
	v_mfma_f32_16x16x32_bf16 v[6:9], v[150:153], v[212:215], v[6:9]
	v_mfma_f32_16x16x32_bf16 v[30:33], v[154:157], v[178:181], v[30:33]
	v_mfma_f32_16x16x32_bf16 v[26:29], v[162:165], v[178:181], v[26:29]
	v_mfma_f32_16x16x32_bf16 v[18:21], v[162:165], v[200:203], v[18:21]
	v_mfma_f32_16x16x32_bf16 v[22:25], v[154:157], v[200:203], v[22:25]
	v_mfma_f32_16x16x32_bf16 v[14:17], v[154:157], v[208:211], v[14:17]
	v_mfma_f32_16x16x32_bf16 v[10:13], v[162:165], v[208:211], v[10:13]
	v_mfma_f32_16x16x32_bf16 v[2:5], v[162:165], v[216:219], v[2:5]
	v_mfma_f32_16x16x32_bf16 v[6:9], v[154:157], v[216:219], v[6:9]
	s_add_i32 s74, s74, 2
	s_add_u32 s36, s36, 0x100
	s_addc_u32 s37, s37, 0
	s_add_u32 s72, s72, 0x100
	s_addc_u32 s73, s73, 0
	s_cmp_gt_u32 s74, 13
	s_setprio 0
	s_barrier
	s_cbranch_scc0 .LBB0_541
	v_readlane_b32 s74, v255, 3
	s_and_b64 vcc, exec, s[10:11]
	v_readlane_b32 s75, v255, 4
	s_mov_b32 s58, 0x19b00000
	v_readlane_b32 s59, v255, 10
	s_mov_b32 s60, 0xff61b1e6
	s_mov_b64 s[62:63], 0x800
	s_mov_b32 s64, 0x3b000000
	s_cbranch_vccz .LBB0_544
	s_barrier

.LBB0_900:
	ds_read_b128 v[2:5], v34
	ds_read_b128 v[6:9], v34 offset:1024
	ds_read_b128 v[10:13], v34 offset:2048
	ds_read_b128 v[14:17], v34 offset:3072
	ds_read_b128 v[178:181], v206
	ds_read_b128 v[182:185], v206 offset:1024
	ds_read_b128 v[196:199], v206 offset:2048
	ds_read_b128 v[200:203], v206 offset:3072
	s_add_u32 s6, s42, 0x200
	s_addc_u32 s7, s43, 0
	s_cmp_eq_u32 s86, 24
	s_cselect_b64 vcc, -1, 0
	s_cselect_b32 s7, s52, s7
	s_cselect_b32 s6, s53, s6
	v_cndmask_b32_e32 v21, v19, v195, vcc
	v_cndmask_b32_e32 v20, v18, v194, vcc
	s_mov_b32 m0, s84
	v_lshl_add_u64 v[30:31], s[42:43], 0, v[190:191]
	ds_read_b128 v[22:25], v189
	ds_read_b128 v[26:29], v189 offset:1024
	ds_read_b128 v[210:213], v189 offset:2048
	ds_read_b128 v[214:217], v189 offset:3072
	ds_read_b128 v[222:225], v189 offset:4096
	ds_read_b128 v[226:229], v189 offset:5120
	ds_read_b128 v[230:233], v189 offset:6144
	ds_read_b128 v[234:237], v189 offset:7168
	global_load_lds_dwordx4 v[30:31], off
	v_lshl_add_u64 v[30:31], s[42:43], 0, v[192:193]
	s_mov_b32 m0, s85
	s_nop 0
	global_load_lds_dwordx4 v[30:31], off
	s_waitcnt vmcnt(8)
	s_waitcnt lgkmcnt(0)
	s_barrier
	s_setprio 1
	s_waitcnt lgkmcnt(0)
	v_mfma_f32_16x16x128_f8f6f4 v[160:163], v[2:9], v[22:29], v[160:163]
	v_mfma_f32_16x16x128_f8f6f4 v[156:159], v[10:17], v[22:29], v[156:159]
	v_mfma_f32_16x16x128_f8f6f4 v[148:151], v[10:17], v[210:217], v[148:151]
	v_mfma_f32_16x16x128_f8f6f4 v[152:155], v[2:9], v[210:217], v[152:155]
	v_mfma_f32_16x16x128_f8f6f4 v[144:147], v[2:9], v[222:229], v[144:147]
	v_mfma_f32_16x16x128_f8f6f4 v[140:143], v[10:17], v[222:229], v[140:143]
	v_mfma_f32_16x16x128_f8f6f4 v[132:135], v[10:17], v[230:237], v[132:135]
	v_mfma_f32_16x16x128_f8f6f4 v[136:139], v[2:9], v[230:237], v[136:139]
	s_setprio 0
	s_setprio 1
	v_mfma_f32_16x16x128_f8f6f4 v[128:131], v[178:185], v[22:29], v[128:131]
	v_mfma_f32_16x16x128_f8f6f4 v[124:127], v[196:203], v[22:29], v[124:127]
	v_mfma_f32_16x16x128_f8f6f4 v[116:119], v[196:203], v[210:217], v[116:119]
	v_mfma_f32_16x16x128_f8f6f4 v[120:123], v[178:185], v[210:217], v[120:123]
	v_mfma_f32_16x16x128_f8f6f4 v[112:115], v[178:185], v[222:229], v[112:115]
	v_mfma_f32_16x16x128_f8f6f4 v[108:111], v[196:203], v[222:229], v[108:111]
	v_mfma_f32_16x16x128_f8f6f4 v[100:103], v[196:203], v[230:237], v[100:103]
	v_mfma_f32_16x16x128_f8f6f4 v[104:107], v[178:185], v[230:237], v[104:107]
	s_setprio 0
	s_barrier
	s_mov_b32 m0, s54
	v_lshl_add_u64 v[22:23], v[20:21], 0, v[172:173]
	ds_read_b128 v[210:213], v189 offset:16384
	ds_read_b128 v[214:217], v189 offset:17408
	ds_read_b128 v[222:225], v189 offset:18432
	ds_read_b128 v[226:229], v189 offset:19456
	ds_read_b128 v[230:233], v189 offset:20480
	ds_read_b128 v[234:237], v189 offset:21504
	ds_read_b128 v[238:241], v189 offset:22528
	ds_read_b128 v[242:245], v189 offset:23552
	global_load_lds_dwordx4 v[22:23], off
	v_lshl_add_u64 v[24:25], v[20:21], 0, v[168:169]
	s_mov_b32 m0, s55
	v_lshl_add_u64 v[26:27], v[20:21], 0, s[2:3]
	global_load_lds_dwordx4 v[24:25], off
	v_lshl_add_u64 v[28:29], v[26:27], 0, v[172:173]
	s_mov_b32 m0, s65
	v_lshl_add_u64 v[26:27], v[26:27], 0, v[168:169]
	global_load_lds_dwordx4 v[28:29], off
	s_mov_b32 m0, s67
	v_lshl_add_u64 v[28:29], s[6:7], 0, v[170:171]
	global_load_lds_dwordx4 v[26:27], off
	v_lshl_add_u64 v[26:27], s[6:7], 0, v[174:175]
	s_mov_b32 m0, s72
	s_nop 0
	global_load_lds_dwordx4 v[26:27], off
	s_mov_b32 m0, s73
	s_nop 0
	global_load_lds_dwordx4 v[28:29], off
	s_waitcnt vmcnt(8)
	s_waitcnt lgkmcnt(0)
	s_barrier
	s_setprio 1
	s_waitcnt lgkmcnt(0)
	v_mfma_f32_16x16x128_f8f6f4 v[96:99], v[2:9], v[210:217], v[96:99]
	v_mfma_f32_16x16x128_f8f6f4 v[92:95], v[10:17], v[210:217], v[92:95]
	v_mfma_f32_16x16x128_f8f6f4 v[84:87], v[10:17], v[222:229], v[84:87]
	v_mfma_f32_16x16x128_f8f6f4 v[88:91], v[2:9], v[222:229], v[88:91]
	v_mfma_f32_16x16x128_f8f6f4 v[80:83], v[2:9], v[230:237], v[80:83]
	v_mfma_f32_16x16x128_f8f6f4 v[76:79], v[10:17], v[230:237], v[76:79]
	v_mfma_f32_16x16x128_f8f6f4 v[68:71], v[10:17], v[238:245], v[68:71]
	v_mfma_f32_16x16x128_f8f6f4 v[72:75], v[2:9], v[238:245], v[72:75]
	s_setprio 0
	s_setprio 1
	v_mfma_f32_16x16x128_f8f6f4 v[64:67], v[178:185], v[210:217], v[64:67]
	v_mfma_f32_16x16x128_f8f6f4 v[60:63], v[196:203], v[210:217], v[60:63]
	v_mfma_f32_16x16x128_f8f6f4 v[52:55], v[196:203], v[222:229], v[52:55]
	v_mfma_f32_16x16x128_f8f6f4 v[56:59], v[178:185], v[222:229], v[56:59]
	v_mfma_f32_16x16x128_f8f6f4 v[48:51], v[178:185], v[230:237], v[48:51]
	v_mfma_f32_16x16x128_f8f6f4 v[44:47], v[196:203], v[230:237], v[44:47]
	v_mfma_f32_16x16x128_f8f6f4 v[36:39], v[196:203], v[238:245], v[36:39]
	v_mfma_f32_16x16x128_f8f6f4 v[40:43], v[178:185], v[238:245], v[40:43]
	s_setprio 0
	s_barrier
	ds_read_b128 v[178:181], v207
	ds_read_b128 v[182:185], v207 offset:1024
	ds_read_b128 v[196:199], v207 offset:2048
	ds_read_b128 v[200:203], v207 offset:3072
	ds_read_b128 v[10:13], v208
	ds_read_b128 v[14:17], v208 offset:1024
	ds_read_b128 v[2:5], v208 offset:2048
	ds_read_b128 v[6:9], v208 offset:3072
	s_add_u32 s6, s6, 0x70000
	s_addc_u32 s7, s7, 0
	s_mov_b32 m0, s74
	v_lshl_add_u64 v[30:31], s[6:7], 0, v[174:175]
	ds_read_b128 v[210:213], v189 offset:32768
	ds_read_b128 v[214:217], v189 offset:33792
	ds_read_b128 v[222:225], v189 offset:34816
	ds_read_b128 v[226:229], v189 offset:35840
	ds_read_b128 v[230:233], v189 offset:36864
	ds_read_b128 v[234:237], v189 offset:37888
	ds_read_b128 v[238:241], v189 offset:38912
	ds_read_b128 v[242:245], v189 offset:39936
	global_load_lds_dwordx4 v[30:31], off
	v_lshl_add_u64 v[30:31], s[6:7], 0, v[170:171]
	s_mov_b32 m0, s75
	s_nop 0
	global_load_lds_dwordx4 v[30:31], off
	s_waitcnt vmcnt(8)
	s_waitcnt lgkmcnt(0)
	s_barrier
	s_setprio 1
	s_waitcnt lgkmcnt(0)
	v_mfma_f32_16x16x128_f8f6f4 v[160:163], v[178:185], v[210:217], v[160:163]
	v_mfma_f32_16x16x128_f8f6f4 v[156:159], v[196:203], v[210:217], v[156:159]
	v_mfma_f32_16x16x128_f8f6f4 v[148:151], v[196:203], v[222:229], v[148:151]
	v_mfma_f32_16x16x128_f8f6f4 v[152:155], v[178:185], v[222:229], v[152:155]
	v_mfma_f32_16x16x128_f8f6f4 v[144:147], v[178:185], v[230:237], v[144:147]
	v_mfma_f32_16x16x128_f8f6f4 v[140:143], v[196:203], v[230:237], v[140:143]
	v_mfma_f32_16x16x128_f8f6f4 v[132:135], v[196:203], v[238:245], v[132:135]
	v_mfma_f32_16x16x128_f8f6f4 v[136:139], v[178:185], v[238:245], v[136:139]
	s_setprio 0
	s_setprio 1
	v_mfma_f32_16x16x128_f8f6f4 v[128:131], v[10:17], v[210:217], v[128:131]
	v_mfma_f32_16x16x128_f8f6f4 v[124:127], v[2:9], v[210:217], v[124:127]
	v_mfma_f32_16x16x128_f8f6f4 v[116:119], v[2:9], v[222:229], v[116:119]
	v_mfma_f32_16x16x128_f8f6f4 v[120:123], v[10:17], v[222:229], v[120:123]
	v_mfma_f32_16x16x128_f8f6f4 v[112:115], v[10:17], v[230:237], v[112:115]
	v_mfma_f32_16x16x128_f8f6f4 v[108:111], v[2:9], v[230:237], v[108:111]
	v_mfma_f32_16x16x128_f8f6f4 v[100:103], v[2:9], v[238:245], v[100:103]
	v_mfma_f32_16x16x128_f8f6f4 v[104:107], v[10:17], v[238:245], v[104:107]
	s_setprio 0
	s_barrier
	s_mov_b32 m0, s50
	v_lshl_add_u64 v[22:23], v[22:23], 0, s[18:19]
	ds_read_b128 v[210:213], v189 offset:49152
	ds_read_b128 v[214:217], v189 offset:50176
	ds_read_b128 v[222:225], v189 offset:51200
	ds_read_b128 v[226:229], v189 offset:52224
	ds_read_b128 v[230:233], v189 offset:53248
	ds_read_b128 v[234:237], v189 offset:54272
	ds_read_b128 v[238:241], v189 offset:55296
	ds_read_b128 v[242:245], v189 offset:56320
	global_load_lds_dwordx4 v[22:23], off
	v_lshl_add_u64 v[22:23], v[24:25], 0, s[18:19]
	s_mov_b32 m0, s51
	v_lshl_add_u64 v[20:21], v[20:21], 0, s[34:35]
	global_load_lds_dwordx4 v[22:23], off
	v_lshl_add_u64 v[22:23], v[20:21], 0, v[172:173]
	s_mov_b32 m0, s63
	v_lshl_add_u64 v[20:21], v[20:21], 0, v[168:169]
	global_load_lds_dwordx4 v[22:23], off
	s_mov_b32 m0, s64
	s_nop 0
	global_load_lds_dwordx4 v[20:21], off
	v_lshl_add_u64 v[20:21], v[26:27], 0, s[18:19]
	s_mov_b32 m0, s77
	s_nop 0
	global_load_lds_dwordx4 v[20:21], off
	v_lshl_add_u64 v[20:21], v[28:29], 0, s[18:19]
	s_mov_b32 m0, s78
	s_nop 0
	global_load_lds_dwordx4 v[20:21], off
	s_waitcnt vmcnt(8)
	s_waitcnt lgkmcnt(0)
	s_barrier
	s_setprio 1
	s_waitcnt lgkmcnt(0)
	v_mfma_f32_16x16x128_f8f6f4 v[96:99], v[178:185], v[210:217], v[96:99]
	v_mfma_f32_16x16x128_f8f6f4 v[92:95], v[196:203], v[210:217], v[92:95]
	v_mfma_f32_16x16x128_f8f6f4 v[84:87], v[196:203], v[222:229], v[84:87]
	v_mfma_f32_16x16x128_f8f6f4 v[88:91], v[178:185], v[222:229], v[88:91]
	v_mfma_f32_16x16x128_f8f6f4 v[80:83], v[178:185], v[230:237], v[80:83]
	v_mfma_f32_16x16x128_f8f6f4 v[76:79], v[196:203], v[230:237], v[76:79]
	v_mfma_f32_16x16x128_f8f6f4 v[68:71], v[196:203], v[238:245], v[68:71]
	v_mfma_f32_16x16x128_f8f6f4 v[72:75], v[178:185], v[238:245], v[72:75]
	s_setprio 0
	s_setprio 1
	v_mfma_f32_16x16x128_f8f6f4 v[64:67], v[10:17], v[210:217], v[64:67]
	v_mfma_f32_16x16x128_f8f6f4 v[60:63], v[2:9], v[210:217], v[60:63]
	v_mfma_f32_16x16x128_f8f6f4 v[52:55], v[2:9], v[222:229], v[52:55]
	v_mfma_f32_16x16x128_f8f6f4 v[56:59], v[10:17], v[222:229], v[56:59]
	v_mfma_f32_16x16x128_f8f6f4 v[48:51], v[10:17], v[230:237], v[48:51]
	v_mfma_f32_16x16x128_f8f6f4 v[44:47], v[2:9], v[230:237], v[44:47]
	v_mfma_f32_16x16x128_f8f6f4 v[36:39], v[2:9], v[238:245], v[36:39]
	v_mfma_f32_16x16x128_f8f6f4 v[40:43], v[10:17], v[238:245], v[40:43]
	s_add_i32 s86, s86, 2
	s_add_u32 s42, s42, 0x100
	s_addc_u32 s43, s43, 0
	s_cmp_gt_u32 s86, 25
	v_lshl_add_u64 v[18:19], v[18:19], 0, s[28:29]
	s_setprio 0
	s_barrier
	s_cbranch_scc0 .LBB0_900
	s_and_b64 vcc, exec, s[36:37]
	s_mov_b64 s[84:85], s[24:25]
	s_cbranch_vccz .LBB0_903
	s_barrier

.LBB0_1087:
	ds_read_b128 v[2:5], v198
	ds_read_b128 v[6:9], v198 offset:1024
	ds_read_b128 v[10:13], v198 offset:2048
	ds_read_b128 v[14:17], v198 offset:3072
	ds_read_b128 v[18:21], v199
	ds_read_b128 v[22:25], v199 offset:1024
	ds_read_b128 v[26:29], v199 offset:2048
	ds_read_b128 v[30:33], v199 offset:3072
	s_add_u32 s14, s30, 0xfffe0080
	s_addc_u32 s22, s31, -1
	s_cmp_eq_u32 s70, 4
	s_cselect_b32 s37, s54, s22
	s_cselect_b32 s36, s55, s14
	s_cselect_b32 s23, s56, s69
	s_cselect_b32 s22, s57, s68
	s_mov_b32 m0, s58
	v_lshl_add_u64 v[174:175], s[30:31], 0, v[170:171]
	ds_read_b128 v[202:205], v197
	ds_read_b128 v[206:209], v197 offset:1024
	ds_read_b128 v[222:225], v197 offset:2048
	ds_read_b128 v[226:229], v197 offset:3072
	ds_read_b128 v[230:233], v197 offset:4096
	ds_read_b128 v[234:237], v197 offset:5120
	ds_read_b128 v[238:241], v197 offset:6144
	ds_read_b128 v[242:245], v197 offset:7168
	global_load_lds_dwordx4 v[174:175], off
	v_lshl_add_u64 v[174:175], s[30:31], 0, v[172:173]
	s_mov_b32 m0, s59
	s_nop 0
	global_load_lds_dwordx4 v[174:175], off
	s_waitcnt vmcnt(8)
	s_waitcnt lgkmcnt(0)
	s_barrier
	s_setprio 1
	s_waitcnt lgkmcnt(0)
	v_mfma_f32_16x16x128_f8f6f4 v[160:163], v[2:9], v[202:209], v[160:163]
	v_mfma_f32_16x16x128_f8f6f4 v[156:159], v[10:17], v[202:209], v[156:159]
	v_mfma_f32_16x16x128_f8f6f4 v[148:151], v[10:17], v[222:229], v[148:151]
	v_mfma_f32_16x16x128_f8f6f4 v[152:155], v[2:9], v[222:229], v[152:155]
	v_mfma_f32_16x16x128_f8f6f4 v[144:147], v[2:9], v[230:237], v[144:147]
	v_mfma_f32_16x16x128_f8f6f4 v[140:143], v[10:17], v[230:237], v[140:143]
	v_mfma_f32_16x16x128_f8f6f4 v[132:135], v[10:17], v[238:245], v[132:135]
	v_mfma_f32_16x16x128_f8f6f4 v[136:139], v[2:9], v[238:245], v[136:139]
	s_setprio 0
	s_setprio 1
	v_mfma_f32_16x16x128_f8f6f4 v[128:131], v[18:25], v[202:209], v[128:131]
	v_mfma_f32_16x16x128_f8f6f4 v[124:127], v[26:33], v[202:209], v[124:127]
	v_mfma_f32_16x16x128_f8f6f4 v[116:119], v[26:33], v[222:229], v[116:119]
	v_mfma_f32_16x16x128_f8f6f4 v[120:123], v[18:25], v[222:229], v[120:123]
	v_mfma_f32_16x16x128_f8f6f4 v[112:115], v[18:25], v[230:237], v[112:115]
	v_mfma_f32_16x16x128_f8f6f4 v[108:111], v[26:33], v[230:237], v[108:111]
	v_mfma_f32_16x16x128_f8f6f4 v[100:103], v[26:33], v[238:245], v[100:103]
	v_mfma_f32_16x16x128_f8f6f4 v[104:107], v[18:25], v[238:245], v[104:107]
	s_setprio 0
	s_barrier
	s_mov_b32 m0, s60
	v_lshl_add_u64 v[174:175], s[22:23], 0, v[34:35]
	s_add_u32 s72, s22, 0x20000
	ds_read_b128 v[202:205], v197 offset:16384
	ds_read_b128 v[206:209], v197 offset:17408
	ds_read_b128 v[222:225], v197 offset:18432
	ds_read_b128 v[226:229], v197 offset:19456
	ds_read_b128 v[230:233], v197 offset:20480
	ds_read_b128 v[234:237], v197 offset:21504
	ds_read_b128 v[238:241], v197 offset:22528
	ds_read_b128 v[242:245], v197 offset:23552
	global_load_lds_dwordx4 v[174:175], off
	v_lshl_add_u64 v[190:191], s[22:23], 0, v[164:165]
	s_mov_b32 m0, s61
	s_addc_u32 s73, s23, 0
	global_load_lds_dwordx4 v[190:191], off
	v_lshl_add_u64 v[178:179], s[72:73], 0, v[34:35]
	s_mov_b32 m0, s62
	v_lshl_add_u64 v[192:193], s[36:37], 0, v[168:169]
	global_load_lds_dwordx4 v[178:179], off
	v_lshl_add_u64 v[178:179], s[72:73], 0, v[164:165]
	s_mov_b32 m0, s63
	v_lshl_add_u64 v[194:195], s[36:37], 0, v[166:167]
	global_load_lds_dwordx4 v[178:179], off
	s_mov_b32 m0, s41
	s_nop 0
	global_load_lds_dwordx4 v[192:193], off
	s_mov_b32 m0, s42
	s_nop 0
	global_load_lds_dwordx4 v[194:195], off
	s_waitcnt vmcnt(8)
	s_waitcnt lgkmcnt(0)
	s_barrier
	s_setprio 1
	s_waitcnt lgkmcnt(0)
	v_mfma_f32_16x16x128_f8f6f4 v[96:99], v[2:9], v[202:209], v[96:99]
	v_mfma_f32_16x16x128_f8f6f4 v[92:95], v[10:17], v[202:209], v[92:95]
	v_mfma_f32_16x16x128_f8f6f4 v[84:87], v[10:17], v[222:229], v[84:87]
	v_mfma_f32_16x16x128_f8f6f4 v[88:91], v[2:9], v[222:229], v[88:91]
	v_mfma_f32_16x16x128_f8f6f4 v[80:83], v[2:9], v[230:237], v[80:83]
	v_mfma_f32_16x16x128_f8f6f4 v[76:79], v[10:17], v[230:237], v[76:79]
	v_mfma_f32_16x16x128_f8f6f4 v[68:71], v[10:17], v[238:245], v[68:71]
	v_mfma_f32_16x16x128_f8f6f4 v[72:75], v[2:9], v[238:245], v[72:75]
	s_setprio 0
	s_setprio 1
	v_mfma_f32_16x16x128_f8f6f4 v[64:67], v[18:25], v[202:209], v[64:67]
	v_mfma_f32_16x16x128_f8f6f4 v[60:63], v[26:33], v[202:209], v[60:63]
	v_mfma_f32_16x16x128_f8f6f4 v[52:55], v[26:33], v[222:229], v[52:55]
	v_mfma_f32_16x16x128_f8f6f4 v[56:59], v[18:25], v[222:229], v[56:59]
	v_mfma_f32_16x16x128_f8f6f4 v[48:51], v[18:25], v[230:237], v[48:51]
	v_mfma_f32_16x16x128_f8f6f4 v[44:47], v[26:33], v[230:237], v[44:47]
	v_mfma_f32_16x16x128_f8f6f4 v[36:39], v[26:33], v[238:245], v[36:39]
	v_mfma_f32_16x16x128_f8f6f4 v[40:43], v[18:25], v[238:245], v[40:43]
	s_setprio 0
	s_barrier
	ds_read_b128 v[26:29], v200
	ds_read_b128 v[30:33], v200 offset:1024
	ds_read_b128 v[18:21], v200 offset:2048
	ds_read_b128 v[22:25], v200 offset:3072
	ds_read_b128 v[10:13], v201
	ds_read_b128 v[14:17], v201 offset:1024
	ds_read_b128 v[2:5], v201 offset:2048
	ds_read_b128 v[6:9], v201 offset:3072
	s_add_u32 s36, s36, 0x20000
	s_addc_u32 s37, s37, 0
	s_mov_b32 m0, s43
	v_lshl_add_u64 v[178:179], s[36:37], 0, v[168:169]
	ds_read_b128 v[202:205], v197 offset:32768
	ds_read_b128 v[206:209], v197 offset:33792
	ds_read_b128 v[222:225], v197 offset:34816
	ds_read_b128 v[226:229], v197 offset:35840
	ds_read_b128 v[230:233], v197 offset:36864
	ds_read_b128 v[234:237], v197 offset:37888
	ds_read_b128 v[238:241], v197 offset:38912
	ds_read_b128 v[242:245], v197 offset:39936
	global_load_lds_dwordx4 v[178:179], off
	v_lshl_add_u64 v[178:179], s[36:37], 0, v[166:167]
	s_mov_b32 m0, s44
	s_nop 0
	global_load_lds_dwordx4 v[178:179], off
	s_waitcnt vmcnt(8)
	s_waitcnt lgkmcnt(0)
	s_barrier
	s_setprio 1
	s_waitcnt lgkmcnt(0)
	v_mfma_f32_16x16x128_f8f6f4 v[160:163], v[26:33], v[202:209], v[160:163]
	v_mfma_f32_16x16x128_f8f6f4 v[156:159], v[18:25], v[202:209], v[156:159]
	v_mfma_f32_16x16x128_f8f6f4 v[148:151], v[18:25], v[222:229], v[148:151]
	v_mfma_f32_16x16x128_f8f6f4 v[152:155], v[26:33], v[222:229], v[152:155]
	v_mfma_f32_16x16x128_f8f6f4 v[144:147], v[26:33], v[230:237], v[144:147]
	v_mfma_f32_16x16x128_f8f6f4 v[140:143], v[18:25], v[230:237], v[140:143]
	v_mfma_f32_16x16x128_f8f6f4 v[132:135], v[18:25], v[238:245], v[132:135]
	v_mfma_f32_16x16x128_f8f6f4 v[136:139], v[26:33], v[238:245], v[136:139]
	s_setprio 0
	s_setprio 1
	v_mfma_f32_16x16x128_f8f6f4 v[128:131], v[10:17], v[202:209], v[128:131]
	v_mfma_f32_16x16x128_f8f6f4 v[124:127], v[2:9], v[202:209], v[124:127]
	v_mfma_f32_16x16x128_f8f6f4 v[116:119], v[2:9], v[222:229], v[116:119]
	v_mfma_f32_16x16x128_f8f6f4 v[120:123], v[10:17], v[222:229], v[120:123]
	v_mfma_f32_16x16x128_f8f6f4 v[112:115], v[10:17], v[230:237], v[112:115]
	v_mfma_f32_16x16x128_f8f6f4 v[108:111], v[2:9], v[230:237], v[108:111]
	v_mfma_f32_16x16x128_f8f6f4 v[100:103], v[2:9], v[238:245], v[100:103]
	v_mfma_f32_16x16x128_f8f6f4 v[104:107], v[10:17], v[238:245], v[104:107]
	s_setprio 0
	s_barrier
	s_mov_b32 m0, s64
	v_lshl_add_u64 v[174:175], v[174:175], 0, s[18:19]
	s_add_u32 s22, s22, 0x20080
	ds_read_b128 v[202:205], v197 offset:49152
	ds_read_b128 v[206:209], v197 offset:50176
	ds_read_b128 v[222:225], v197 offset:51200
	ds_read_b128 v[226:229], v197 offset:52224
	ds_read_b128 v[230:233], v197 offset:53248
	ds_read_b128 v[234:237], v197 offset:54272
	ds_read_b128 v[238:241], v197 offset:55296
	ds_read_b128 v[242:245], v197 offset:56320
	global_load_lds_dwordx4 v[174:175], off
	v_lshl_add_u64 v[174:175], v[190:191], 0, s[18:19]
	s_mov_b32 m0, s65
	s_addc_u32 s23, s23, 0
	global_load_lds_dwordx4 v[174:175], off
	v_lshl_add_u64 v[174:175], s[22:23], 0, v[34:35]
	s_mov_b32 m0, s66
	s_nop 0
	global_load_lds_dwordx4 v[174:175], off
	v_lshl_add_u64 v[174:175], s[22:23], 0, v[164:165]
	s_mov_b32 m0, s67
	s_nop 0
	global_load_lds_dwordx4 v[174:175], off
	v_lshl_add_u64 v[174:175], v[192:193], 0, s[18:19]
	s_mov_b32 m0, s47
	s_nop 0
	global_load_lds_dwordx4 v[174:175], off
	v_lshl_add_u64 v[174:175], v[194:195], 0, s[18:19]
	s_mov_b32 m0, s48
	s_nop 0
	global_load_lds_dwordx4 v[174:175], off
	s_waitcnt vmcnt(8)
	s_waitcnt lgkmcnt(0)
	s_barrier
	s_setprio 1
	s_waitcnt lgkmcnt(0)
	v_mfma_f32_16x16x128_f8f6f4 v[96:99], v[26:33], v[202:209], v[96:99]
	v_mfma_f32_16x16x128_f8f6f4 v[92:95], v[18:25], v[202:209], v[92:95]
	v_mfma_f32_16x16x128_f8f6f4 v[84:87], v[18:25], v[222:229], v[84:87]
	v_mfma_f32_16x16x128_f8f6f4 v[88:91], v[26:33], v[222:229], v[88:91]
	v_mfma_f32_16x16x128_f8f6f4 v[80:83], v[26:33], v[230:237], v[80:83]
	v_mfma_f32_16x16x128_f8f6f4 v[76:79], v[18:25], v[230:237], v[76:79]
	v_mfma_f32_16x16x128_f8f6f4 v[68:71], v[18:25], v[238:245], v[68:71]
	v_mfma_f32_16x16x128_f8f6f4 v[72:75], v[26:33], v[238:245], v[72:75]
	s_setprio 0
	s_setprio 1
	v_mfma_f32_16x16x128_f8f6f4 v[64:67], v[10:17], v[202:209], v[64:67]
	v_mfma_f32_16x16x128_f8f6f4 v[60:63], v[2:9], v[202:209], v[60:63]
	v_mfma_f32_16x16x128_f8f6f4 v[52:55], v[2:9], v[222:229], v[52:55]
	v_mfma_f32_16x16x128_f8f6f4 v[56:59], v[10:17], v[222:229], v[56:59]
	v_mfma_f32_16x16x128_f8f6f4 v[48:51], v[10:17], v[230:237], v[48:51]
	v_mfma_f32_16x16x128_f8f6f4 v[44:47], v[2:9], v[230:237], v[44:47]
	v_mfma_f32_16x16x128_f8f6f4 v[36:39], v[2:9], v[238:245], v[36:39]
	v_mfma_f32_16x16x128_f8f6f4 v[40:43], v[10:17], v[238:245], v[40:43]
	s_add_i32 s70, s70, 2
	s_add_u32 s30, s30, 0x100
	s_addc_u32 s31, s31, 0
	s_add_u32 s68, s68, 0x100
	s_addc_u32 s69, s69, 0
	s_cmp_gt_u32 s70, 5
	s_setprio 0
	s_barrier
	s_cbranch_scc0 .LBB0_1087

.LBB0_1160:
	s_add_u32 s22, s30, 0x100
	s_addc_u32 s23, s31, 0
	s_add_i32 s65, 0, 0x10000
	s_cmp_eq_u32 s64, 18
	s_cselect_b32 s41, s58, s23
	s_cselect_b32 s40, s59, s22
	s_cselect_b32 s37, s60, s63
	s_cselect_b32 s36, s61, s62
	s_add_i32 s66, 0, 0x14000
	v_add_u32_e32 v2, s65, v222
	v_add_u32_e32 v6, s66, v222
	ds_read_b128 v[26:29], v2
	ds_read_b128 v[30:33], v2 offset:1024
	ds_read_b128 v[18:21], v2 offset:2048
	ds_read_b128 v[22:25], v2 offset:3072
	ds_read_b128 v[10:13], v6
	ds_read_b128 v[14:17], v6 offset:1024
	ds_read_b128 v[2:5], v6 offset:2048
	ds_read_b128 v[6:9], v6 offset:3072
	v_lshl_add_u64 v[174:175], s[30:31], 0, v[170:171]
	s_add_i32 m0, s43, 0xc000
	ds_read_b128 v[190:193], v223
	ds_read_b128 v[194:197], v223 offset:1024
	ds_read_b128 v[198:201], v223 offset:2048
	ds_read_b128 v[202:205], v223 offset:3072
	ds_read_b128 v[224:227], v223 offset:4096
	ds_read_b128 v[228:231], v223 offset:5120
	ds_read_b128 v[232:235], v223 offset:6144
	ds_read_b128 v[236:239], v223 offset:7168
	global_load_lds_dwordx4 v[174:175], off
	v_lshl_add_u64 v[174:175], s[30:31], 0, v[172:173]
	s_add_i32 m0, s43, 0xe000
	s_nop 0
	global_load_lds_dwordx4 v[174:175], off
	s_waitcnt vmcnt(8)
	s_waitcnt lgkmcnt(0)
	s_barrier
	s_setprio 1
	s_waitcnt lgkmcnt(0)
	v_mfma_f32_16x16x128_f8f6f4 v[160:163], v[26:33], v[190:197], v[160:163]
	v_mfma_f32_16x16x128_f8f6f4 v[156:159], v[18:25], v[190:197], v[156:159]
	v_mfma_f32_16x16x128_f8f6f4 v[140:143], v[18:25], v[198:205], v[140:143]
	v_mfma_f32_16x16x128_f8f6f4 v[144:147], v[26:33], v[198:205], v[144:147]
	v_mfma_f32_16x16x128_f8f6f4 v[132:135], v[26:33], v[224:231], v[132:135]
	v_mfma_f32_16x16x128_f8f6f4 v[124:127], v[18:25], v[224:231], v[124:127]
	v_mfma_f32_16x16x128_f8f6f4 v[108:111], v[18:25], v[232:239], v[108:111]
	v_mfma_f32_16x16x128_f8f6f4 v[116:119], v[26:33], v[232:239], v[116:119]
	s_setprio 0
	s_setprio 1
	v_mfma_f32_16x16x128_f8f6f4 v[152:155], v[10:17], v[190:197], v[152:155]
	v_mfma_f32_16x16x128_f8f6f4 v[148:151], v[2:9], v[190:197], v[148:151]
	v_mfma_f32_16x16x128_f8f6f4 v[128:131], v[2:9], v[198:205], v[128:131]
	v_mfma_f32_16x16x128_f8f6f4 v[136:139], v[10:17], v[198:205], v[136:139]
	v_mfma_f32_16x16x128_f8f6f4 v[120:123], v[10:17], v[224:231], v[120:123]
	v_mfma_f32_16x16x128_f8f6f4 v[112:115], v[2:9], v[224:231], v[112:115]
	v_mfma_f32_16x16x128_f8f6f4 v[100:103], v[2:9], v[232:239], v[100:103]
	v_mfma_f32_16x16x128_f8f6f4 v[104:107], v[10:17], v[232:239], v[104:107]
	s_setprio 0
	s_barrier
	s_add_i32 s14, s65, s42
	v_lshl_add_u64 v[174:175], s[36:37], 0, v[34:35]
	s_mov_b32 m0, s14
	ds_read_b128 v[196:199], v223 offset:16384
	ds_read_b128 v[200:203], v223 offset:17408
	ds_read_b128 v[204:207], v223 offset:18432
	ds_read_b128 v[208:211], v223 offset:19456
	ds_read_b128 v[224:227], v223 offset:20480
	ds_read_b128 v[228:231], v223 offset:21504
	ds_read_b128 v[232:235], v223 offset:22528
	ds_read_b128 v[236:239], v223 offset:23552
	global_load_lds_dwordx4 v[174:175], off
	s_add_i32 m0, s14, 0x2000
	s_add_u32 s30, s36, 0x58000
	v_lshl_add_u64 v[190:191], s[36:37], 0, v[164:165]
	s_addc_u32 s31, s37, 0
	s_add_i32 s14, s66, s42
	global_load_lds_dwordx4 v[190:191], off
	v_lshl_add_u64 v[178:179], s[30:31], 0, v[34:35]
	s_mov_b32 m0, s14
	v_lshl_add_u64 v[192:193], s[40:41], 0, v[168:169]
	global_load_lds_dwordx4 v[178:179], off
	v_lshl_add_u64 v[178:179], s[30:31], 0, v[164:165]
	s_add_i32 m0, s14, 0x2000
	v_lshl_add_u64 v[194:195], s[40:41], 0, v[166:167]
	global_load_lds_dwordx4 v[178:179], off
	s_mov_b32 m0, s43
	s_nop 0
	global_load_lds_dwordx4 v[192:193], off
	s_mov_b32 m0, s44
	s_nop 0
	global_load_lds_dwordx4 v[194:195], off
	s_waitcnt vmcnt(8)
	s_waitcnt lgkmcnt(0)
	s_barrier
	s_setprio 1
	s_waitcnt lgkmcnt(0)
	v_mfma_f32_16x16x128_f8f6f4 v[96:99], v[26:33], v[196:203], v[96:99]
	v_mfma_f32_16x16x128_f8f6f4 v[92:95], v[18:25], v[196:203], v[92:95]
	v_mfma_f32_16x16x128_f8f6f4 v[76:79], v[18:25], v[204:211], v[76:79]
	v_mfma_f32_16x16x128_f8f6f4 v[84:87], v[26:33], v[204:211], v[84:87]
	v_mfma_f32_16x16x128_f8f6f4 v[68:71], v[26:33], v[224:231], v[68:71]
	v_mfma_f32_16x16x128_f8f6f4 v[60:63], v[18:25], v[224:231], v[60:63]
	v_mfma_f32_16x16x128_f8f6f4 v[44:47], v[18:25], v[232:239], v[44:47]
	v_mfma_f32_16x16x128_f8f6f4 v[52:55], v[26:33], v[232:239], v[52:55]
	s_setprio 0
	s_setprio 1
	v_mfma_f32_16x16x128_f8f6f4 v[88:91], v[10:17], v[196:203], v[88:91]
	v_mfma_f32_16x16x128_f8f6f4 v[80:83], v[2:9], v[196:203], v[80:83]
	v_mfma_f32_16x16x128_f8f6f4 v[64:67], v[2:9], v[204:211], v[64:67]
	v_mfma_f32_16x16x128_f8f6f4 v[72:75], v[10:17], v[204:211], v[72:75]
	v_mfma_f32_16x16x128_f8f6f4 v[56:59], v[10:17], v[224:231], v[56:59]
	v_mfma_f32_16x16x128_f8f6f4 v[48:51], v[2:9], v[224:231], v[48:51]
	v_mfma_f32_16x16x128_f8f6f4 v[36:39], v[2:9], v[232:239], v[36:39]
	v_mfma_f32_16x16x128_f8f6f4 v[40:43], v[10:17], v[232:239], v[40:43]
	s_setprio 0
	s_barrier
	s_add_i32 s14, 0, 0x18000
	s_add_i32 s65, 0, 0x1c000
	v_add_u32_e32 v14, s14, v222
	v_add_u32_e32 v30, s65, v222
	ds_read_b128 v[2:5], v14
	ds_read_b128 v[6:9], v14 offset:1024
	ds_read_b128 v[10:13], v14 offset:2048
	ds_read_b128 v[14:17], v14 offset:3072
	ds_read_b128 v[18:21], v30
	ds_read_b128 v[22:25], v30 offset:1024
	ds_read_b128 v[26:29], v30 offset:2048
	ds_read_b128 v[30:33], v30 offset:3072
	s_add_u32 s30, s40, 0x58000
	s_addc_u32 s31, s41, 0
	s_mov_b32 m0, s45
	v_lshl_add_u64 v[178:179], s[30:31], 0, v[168:169]
	ds_read_b128 v[196:199], v223 offset:32768
	ds_read_b128 v[200:203], v223 offset:33792
	ds_read_b128 v[204:207], v223 offset:34816
	ds_read_b128 v[208:211], v223 offset:35840
	ds_read_b128 v[224:227], v223 offset:36864
	ds_read_b128 v[228:231], v223 offset:37888
	ds_read_b128 v[232:235], v223 offset:38912
	ds_read_b128 v[236:239], v223 offset:39936
	global_load_lds_dwordx4 v[178:179], off
	v_lshl_add_u64 v[178:179], s[30:31], 0, v[166:167]
	s_mov_b32 m0, s46
	s_nop 0
	global_load_lds_dwordx4 v[178:179], off
	s_waitcnt vmcnt(8)
	s_waitcnt lgkmcnt(0)
	s_barrier
	s_setprio 1
	s_waitcnt lgkmcnt(0)
	v_mfma_f32_16x16x128_f8f6f4 v[160:163], v[2:9], v[196:203], v[160:163]
	v_mfma_f32_16x16x128_f8f6f4 v[156:159], v[10:17], v[196:203], v[156:159]
	v_mfma_f32_16x16x128_f8f6f4 v[140:143], v[10:17], v[204:211], v[140:143]
	v_mfma_f32_16x16x128_f8f6f4 v[144:147], v[2:9], v[204:211], v[144:147]
	v_mfma_f32_16x16x128_f8f6f4 v[132:135], v[2:9], v[224:231], v[132:135]
	v_mfma_f32_16x16x128_f8f6f4 v[124:127], v[10:17], v[224:231], v[124:127]
	v_mfma_f32_16x16x128_f8f6f4 v[108:111], v[10:17], v[232:239], v[108:111]
	v_mfma_f32_16x16x128_f8f6f4 v[116:119], v[2:9], v[232:239], v[116:119]
	s_setprio 0
	s_setprio 1
	v_mfma_f32_16x16x128_f8f6f4 v[152:155], v[18:25], v[196:203], v[152:155]
	v_mfma_f32_16x16x128_f8f6f4 v[148:151], v[26:33], v[196:203], v[148:151]
	v_mfma_f32_16x16x128_f8f6f4 v[128:131], v[26:33], v[204:211], v[128:131]
	v_mfma_f32_16x16x128_f8f6f4 v[136:139], v[18:25], v[204:211], v[136:139]
	v_mfma_f32_16x16x128_f8f6f4 v[120:123], v[18:25], v[224:231], v[120:123]
	v_mfma_f32_16x16x128_f8f6f4 v[112:115], v[26:33], v[224:231], v[112:115]
	v_mfma_f32_16x16x128_f8f6f4 v[100:103], v[26:33], v[232:239], v[100:103]
	v_mfma_f32_16x16x128_f8f6f4 v[104:107], v[18:25], v[232:239], v[104:107]
	s_setprio 0
	s_barrier
	s_add_i32 s14, s14, s42
	v_lshl_add_u64 v[174:175], v[174:175], 0, s[18:19]
	s_mov_b32 m0, s14
	ds_read_b128 v[196:199], v223 offset:49152
	ds_read_b128 v[200:203], v223 offset:50176
	ds_read_b128 v[204:207], v223 offset:51200
	ds_read_b128 v[208:211], v223 offset:52224
	ds_read_b128 v[224:227], v223 offset:53248
	ds_read_b128 v[228:231], v223 offset:54272
	ds_read_b128 v[232:235], v223 offset:55296
	ds_read_b128 v[236:239], v223 offset:56320
	global_load_lds_dwordx4 v[174:175], off
	s_add_i32 m0, s14, 0x2000
	s_add_u32 s30, s36, 0x58080
	v_lshl_add_u64 v[174:175], v[190:191], 0, s[18:19]
	s_addc_u32 s31, s37, 0
	s_add_i32 s14, s65, s42
	global_load_lds_dwordx4 v[174:175], off
	v_lshl_add_u64 v[174:175], s[30:31], 0, v[34:35]
	s_mov_b32 m0, s14
	s_nop 0
	global_load_lds_dwordx4 v[174:175], off
	v_lshl_add_u64 v[174:175], s[30:31], 0, v[164:165]
	s_add_i32 m0, s14, 0x2000
	s_nop 0
	global_load_lds_dwordx4 v[174:175], off
	v_lshl_add_u64 v[174:175], v[192:193], 0, s[18:19]
	s_mov_b32 m0, s51
	s_nop 0
	global_load_lds_dwordx4 v[174:175], off
	v_lshl_add_u64 v[174:175], v[194:195], 0, s[18:19]
	s_mov_b32 m0, s52
	s_nop 0
	global_load_lds_dwordx4 v[174:175], off
	s_waitcnt vmcnt(8)
	s_waitcnt lgkmcnt(0)
	s_barrier
	s_setprio 1
	s_waitcnt lgkmcnt(0)
	v_mfma_f32_16x16x128_f8f6f4 v[96:99], v[2:9], v[196:203], v[96:99]
	v_mfma_f32_16x16x128_f8f6f4 v[92:95], v[10:17], v[196:203], v[92:95]
	v_mfma_f32_16x16x128_f8f6f4 v[76:79], v[10:17], v[204:211], v[76:79]
	v_mfma_f32_16x16x128_f8f6f4 v[84:87], v[2:9], v[204:211], v[84:87]
	v_mfma_f32_16x16x128_f8f6f4 v[68:71], v[2:9], v[224:231], v[68:71]
	v_mfma_f32_16x16x128_f8f6f4 v[60:63], v[10:17], v[224:231], v[60:63]
	v_mfma_f32_16x16x128_f8f6f4 v[44:47], v[10:17], v[232:239], v[44:47]
	v_mfma_f32_16x16x128_f8f6f4 v[52:55], v[2:9], v[232:239], v[52:55]
	s_setprio 0
	s_setprio 1
	v_mfma_f32_16x16x128_f8f6f4 v[88:91], v[18:25], v[196:203], v[88:91]
	v_mfma_f32_16x16x128_f8f6f4 v[80:83], v[26:33], v[196:203], v[80:83]
	v_mfma_f32_16x16x128_f8f6f4 v[64:67], v[26:33], v[204:211], v[64:67]
	v_mfma_f32_16x16x128_f8f6f4 v[72:75], v[18:25], v[204:211], v[72:75]
	v_mfma_f32_16x16x128_f8f6f4 v[56:59], v[18:25], v[224:231], v[56:59]
	v_mfma_f32_16x16x128_f8f6f4 v[48:51], v[26:33], v[224:231], v[48:51]
	v_mfma_f32_16x16x128_f8f6f4 v[36:39], v[26:33], v[232:239], v[36:39]
	v_mfma_f32_16x16x128_f8f6f4 v[40:43], v[18:25], v[232:239], v[40:43]
	s_add_i32 s64, s64, 2
	s_add_u32 s62, s62, 0x100
	s_addc_u32 s63, s63, 0
	s_cmp_gt_u32 s64, 19
	s_mov_b64 s[30:31], s[22:23]
	s_setprio 0
	s_barrier
	s_cbranch_scc0 .LBB0_1160
	s_and_b64 vcc, exec, s[8:9]
	s_mov_b32 s58, 0x19b00000
	v_readlane_b32 s59, v255, 10
	s_mov_b32 s60, 0xff61b1e6
	s_mov_b64 s[62:63], 0x800
	s_cbranch_vccz .LBB0_1163
	s_barrier
